# up-proj seam: first gate load no longer waited alone; P0 w_in items: 8 waves of a WG take 8 adjacent column blocks; up-proj phase: odd workgroups of each XCD start 2 sleeps later to spread the seam ga
# speedup vs baseline: 1.0017x; 1.0017x over previous
.LBB0_1616:
	v_readlane_b32 s98, v254, 6
	s_nop 0
	s_bitcmp1_b32 s98, 3
	s_cbranch_scc0 .Lup_nosleep
	s_sleep 127
	s_sleep 127
